# P11: workgroups without a router-GEMM tile convert the last expert-weight chunk of every workgroup (placement-neutral)
# baseline (speedup 1.0000x reference)
.Lp11_done:
	s_branch .LBB0_3627
	s_nop 0
	s_nop 0
	s_nop 0
	s_nop 0
	s_nop 0
	s_nop 0
	s_nop 0
	s_nop 0
	s_nop 0
	s_nop 0
	s_nop 0
	s_nop 0
	s_nop 0
	s_nop 0
	s_nop 0
	s_nop 0
	s_nop 0
	s_nop 0
	s_nop 0
	s_nop 0
	s_nop 0
	s_nop 0
	s_nop 0
	s_nop 0
	s_nop 0
